# router: read-ahead ds_read placed in the 1-wait-state slot between op_sel-dependent packed FMAs (128 s_nop per pass removed), otherwise v86
# baseline (speedup 1.0000x reference)
; #define LAS __attribute__((address_space(3)))
; __device__ __forceinline__ void phase_norm2(const Params& p, const Ctx& F, const int l) {
;     ...
;         f32x2 lg[16];
;         unsigned wro = (unsigned)(uintptr_t)wr; asm volatile("" : "+v"(wro));
;         const LAS float* wr2 = (const LAS float*)(uintptr_t)wro;
; #pragma unroll
;         for (int e = 0; e < 16; ++e) { f32x2 a = {0.f, 0.f};
; #pragma unroll
;             for (int j = 0; j < 8; ++j) { const f32x4 w = *((const LAS f32x4*)(wr2 + e * DM) + F.lane + 64 * j);
; #pragma unroll
;                 for (int c = 0; c < 4; ++c) a += vv[j][c] * w[c]; }
;             lg[e] = a; }
.LBB0_937:
	s_or_b64 exec, exec, s[12:13]
	v_mov_b32_e32 v1, v35
	s_nop 0
	v_lshl_add_u32 v182, v132, 4, v1
	v_add_u32_e32 v244, 0x10000, v182
	ds_read_b128 v[224:227], v182
	ds_read_b128 v[228:231], v182 offset:1024
	ds_read_b128 v[232:235], v182 offset:2048
	s_waitcnt lgkmcnt(2)
	v_pk_fma_f32 v[156:157], v[124:125], v[224:225], 0 op_sel_hi:[1,0,0]
	ds_read_b128 v[236:239], v182 offset:3072
	v_pk_fma_f32 v[152:153], v[126:127], v[224:225], v[156:157] op_sel:[0,1,0]
	s_nop 0
	v_pk_fma_f32 v[152:153], v[128:129], v[226:227], v[152:153] op_sel_hi:[1,0,1]
	v_mov_b32_e32 v154, v227
	v_pk_fma_f32 v[156:157], v[130:131], v[154:155], v[152:153] op_sel_hi:[1,0,1]
	s_waitcnt lgkmcnt(2)
	v_pk_fma_f32 v[156:157], v[112:113], v[228:229], v[156:157] op_sel_hi:[1,0,1]
	ds_read_b128 v[240:243], v182 offset:4096
	v_pk_fma_f32 v[152:153], v[114:115], v[228:229], v[156:157] op_sel:[0,1,0]
	s_nop 0
	v_pk_fma_f32 v[152:153], v[118:119], v[230:231], v[152:153] op_sel_hi:[1,0,1]
	v_mov_b32_e32 v154, v231
	v_pk_fma_f32 v[156:157], v[122:123], v[154:155], v[152:153] op_sel_hi:[1,0,1]
	s_waitcnt lgkmcnt(2)
	v_pk_fma_f32 v[156:157], v[108:109], v[232:233], v[156:157] op_sel_hi:[1,0,1]
	ds_read_b128 v[224:227], v182 offset:5120
	v_pk_fma_f32 v[152:153], v[110:111], v[232:233], v[156:157] op_sel:[0,1,0]
	s_nop 0
	v_pk_fma_f32 v[152:153], v[116:117], v[234:235], v[152:153] op_sel_hi:[1,0,1]
	v_mov_b32_e32 v154, v235
	v_pk_fma_f32 v[156:157], v[120:121], v[154:155], v[152:153] op_sel_hi:[1,0,1]
	s_waitcnt lgkmcnt(2)
	v_pk_fma_f32 v[156:157], v[96:97], v[236:237], v[156:157] op_sel_hi:[1,0,1]
	ds_read_b128 v[228:231], v182 offset:6144
	v_pk_fma_f32 v[152:153], v[98:99], v[236:237], v[156:157] op_sel:[0,1,0]
	s_nop 0
	v_pk_fma_f32 v[152:153], v[102:103], v[238:239], v[152:153] op_sel_hi:[1,0,1]
	v_mov_b32_e32 v154, v239
	v_pk_fma_f32 v[156:157], v[106:107], v[154:155], v[152:153] op_sel_hi:[1,0,1]
	s_waitcnt lgkmcnt(2)
	v_pk_fma_f32 v[156:157], v[92:93], v[240:241], v[156:157] op_sel_hi:[1,0,1]
	ds_read_b128 v[232:235], v182 offset:7168
	v_pk_fma_f32 v[152:153], v[94:95], v[240:241], v[156:157] op_sel:[0,1,0]
	s_nop 0
	v_pk_fma_f32 v[152:153], v[100:101], v[242:243], v[152:153] op_sel_hi:[1,0,1]
	v_mov_b32_e32 v154, v243
	v_pk_fma_f32 v[156:157], v[104:105], v[154:155], v[152:153] op_sel_hi:[1,0,1]
	s_waitcnt lgkmcnt(2)
	v_pk_fma_f32 v[156:157], v[80:81], v[224:225], v[156:157] op_sel_hi:[1,0,1]
	ds_read_b128 v[236:239], v182 offset:8192
	v_pk_fma_f32 v[152:153], v[82:83], v[224:225], v[156:157] op_sel:[0,1,0]
	s_nop 0
	v_pk_fma_f32 v[152:153], v[86:87], v[226:227], v[152:153] op_sel_hi:[1,0,1]
	v_mov_b32_e32 v154, v227
	v_pk_fma_f32 v[156:157], v[90:91], v[154:155], v[152:153] op_sel_hi:[1,0,1]
	s_waitcnt lgkmcnt(2)
	v_pk_fma_f32 v[156:157], v[76:77], v[228:229], v[156:157] op_sel_hi:[1,0,1]
	ds_read_b128 v[240:243], v182 offset:9216
	v_pk_fma_f32 v[152:153], v[78:79], v[228:229], v[156:157] op_sel:[0,1,0]
	s_nop 0
	v_pk_fma_f32 v[152:153], v[84:85], v[230:231], v[152:153] op_sel_hi:[1,0,1]
	v_mov_b32_e32 v154, v231
	v_pk_fma_f32 v[156:157], v[88:89], v[154:155], v[152:153] op_sel_hi:[1,0,1]
	s_waitcnt lgkmcnt(2)
	v_pk_fma_f32 v[156:157], v[68:69], v[232:233], v[156:157] op_sel_hi:[1,0,1]
	ds_read_b128 v[224:227], v182 offset:10240
	v_pk_fma_f32 v[152:153], v[70:71], v[232:233], v[156:157] op_sel:[0,1,0]
	s_nop 0
	v_pk_fma_f32 v[152:153], v[72:73], v[234:235], v[152:153] op_sel_hi:[1,0,1]
	v_mov_b32_e32 v154, v235
	v_pk_fma_f32 v[152:153], v[74:75], v[154:155], v[152:153] op_sel_hi:[1,0,1]
	s_waitcnt lgkmcnt(2)
	v_pk_fma_f32 v[158:159], v[124:125], v[236:237], 0 op_sel_hi:[1,0,0]
	ds_read_b128 v[228:231], v182 offset:11264
	v_pk_fma_f32 v[154:155], v[126:127], v[236:237], v[158:159] op_sel:[0,1,0]
	s_nop 0
	v_pk_fma_f32 v[154:155], v[128:129], v[238:239], v[154:155] op_sel_hi:[1,0,1]
	v_mov_b32_e32 v156, v239
	v_pk_fma_f32 v[158:159], v[130:131], v[156:157], v[154:155] op_sel_hi:[1,0,1]
	s_waitcnt lgkmcnt(2)
	v_pk_fma_f32 v[158:159], v[112:113], v[240:241], v[158:159] op_sel_hi:[1,0,1]
	ds_read_b128 v[232:235], v182 offset:12288
	v_pk_fma_f32 v[154:155], v[114:115], v[240:241], v[158:159] op_sel:[0,1,0]
	s_nop 0
	v_pk_fma_f32 v[154:155], v[118:119], v[242:243], v[154:155] op_sel_hi:[1,0,1]
	v_mov_b32_e32 v156, v243
	v_pk_fma_f32 v[158:159], v[122:123], v[156:157], v[154:155] op_sel_hi:[1,0,1]
	s_waitcnt lgkmcnt(2)
	v_pk_fma_f32 v[158:159], v[108:109], v[224:225], v[158:159] op_sel_hi:[1,0,1]
	ds_read_b128 v[236:239], v182 offset:13312
	v_pk_fma_f32 v[154:155], v[110:111], v[224:225], v[158:159] op_sel:[0,1,0]
	s_nop 0
	v_pk_fma_f32 v[154:155], v[116:117], v[226:227], v[154:155] op_sel_hi:[1,0,1]
	v_mov_b32_e32 v156, v227
	v_pk_fma_f32 v[158:159], v[120:121], v[156:157], v[154:155] op_sel_hi:[1,0,1]
	s_waitcnt lgkmcnt(2)
	v_pk_fma_f32 v[158:159], v[96:97], v[228:229], v[158:159] op_sel_hi:[1,0,1]
	ds_read_b128 v[240:243], v182 offset:14336
	v_pk_fma_f32 v[154:155], v[98:99], v[228:229], v[158:159] op_sel:[0,1,0]
	s_nop 0
	v_pk_fma_f32 v[154:155], v[102:103], v[230:231], v[154:155] op_sel_hi:[1,0,1]
	v_mov_b32_e32 v156, v231
	v_pk_fma_f32 v[158:159], v[106:107], v[156:157], v[154:155] op_sel_hi:[1,0,1]
	s_waitcnt lgkmcnt(2)
	v_pk_fma_f32 v[158:159], v[92:93], v[232:233], v[158:159] op_sel_hi:[1,0,1]
	ds_read_b128 v[224:227], v182 offset:15360
	v_pk_fma_f32 v[154:155], v[94:95], v[232:233], v[158:159] op_sel:[0,1,0]
	s_nop 0
	v_pk_fma_f32 v[154:155], v[100:101], v[234:235], v[154:155] op_sel_hi:[1,0,1]
	v_mov_b32_e32 v156, v235
	v_pk_fma_f32 v[158:159], v[104:105], v[156:157], v[154:155] op_sel_hi:[1,0,1]
	s_waitcnt lgkmcnt(2)
; #define LAS __attribute__((address_space(3)))
; __device__ __forceinline__ void phase_norm2(const Params& p, const Ctx& F, const int l) {
;     ...
; #pragma unroll
;         for (int e = 0; e < 16; ++e) { f32x2 a = {0.f, 0.f};
; #pragma unroll
;             for (int j = 0; j < 8; ++j) { const f32x4 w = *((const LAS f32x4*)(wr2 + e * DM) + F.lane + 64 * j);
; #pragma unroll
;                 for (int c = 0; c < 4; ++c) a += vv[j][c] * w[c]; }
;             lg[e] = a; }
	v_pk_fma_f32 v[158:159], v[80:81], v[236:237], v[158:159] op_sel_hi:[1,0,1]
	ds_read_b128 v[228:231], v182 offset:16384
	v_pk_fma_f32 v[154:155], v[82:83], v[236:237], v[158:159] op_sel:[0,1,0]
	s_nop 0
	v_pk_fma_f32 v[154:155], v[86:87], v[238:239], v[154:155] op_sel_hi:[1,0,1]
	v_mov_b32_e32 v156, v239
	v_pk_fma_f32 v[158:159], v[90:91], v[156:157], v[154:155] op_sel_hi:[1,0,1]
	s_waitcnt lgkmcnt(2)
	v_pk_fma_f32 v[158:159], v[76:77], v[240:241], v[158:159] op_sel_hi:[1,0,1]
	ds_read_b128 v[232:235], v182 offset:17408
	v_pk_fma_f32 v[154:155], v[78:79], v[240:241], v[158:159] op_sel:[0,1,0]
	s_nop 0
	v_pk_fma_f32 v[154:155], v[84:85], v[242:243], v[154:155] op_sel_hi:[1,0,1]
	v_mov_b32_e32 v156, v243
	v_pk_fma_f32 v[158:159], v[88:89], v[156:157], v[154:155] op_sel_hi:[1,0,1]
	s_waitcnt lgkmcnt(2)
	v_pk_fma_f32 v[158:159], v[68:69], v[224:225], v[158:159] op_sel_hi:[1,0,1]
	ds_read_b128 v[236:239], v182 offset:18432
	v_pk_fma_f32 v[154:155], v[70:71], v[224:225], v[158:159] op_sel:[0,1,0]
	s_nop 0
	v_pk_fma_f32 v[154:155], v[72:73], v[226:227], v[154:155] op_sel_hi:[1,0,1]
	v_mov_b32_e32 v156, v227
	v_pk_fma_f32 v[154:155], v[74:75], v[156:157], v[154:155] op_sel_hi:[1,0,1]
	s_waitcnt lgkmcnt(2)
	v_pk_fma_f32 v[160:161], v[124:125], v[228:229], 0 op_sel_hi:[1,0,0]
	ds_read_b128 v[240:243], v182 offset:19456
	v_pk_fma_f32 v[156:157], v[126:127], v[228:229], v[160:161] op_sel:[0,1,0]
	s_nop 0
	v_pk_fma_f32 v[156:157], v[128:129], v[230:231], v[156:157] op_sel_hi:[1,0,1]
	v_mov_b32_e32 v158, v231
	v_pk_fma_f32 v[160:161], v[130:131], v[158:159], v[156:157] op_sel_hi:[1,0,1]
	s_waitcnt lgkmcnt(2)
	v_pk_fma_f32 v[160:161], v[112:113], v[232:233], v[160:161] op_sel_hi:[1,0,1]
	ds_read_b128 v[224:227], v182 offset:20480
	v_pk_fma_f32 v[156:157], v[114:115], v[232:233], v[160:161] op_sel:[0,1,0]
	s_nop 0
	v_pk_fma_f32 v[156:157], v[118:119], v[234:235], v[156:157] op_sel_hi:[1,0,1]
	v_mov_b32_e32 v158, v235
	v_pk_fma_f32 v[160:161], v[122:123], v[158:159], v[156:157] op_sel_hi:[1,0,1]
	s_waitcnt lgkmcnt(2)
	v_pk_fma_f32 v[160:161], v[108:109], v[236:237], v[160:161] op_sel_hi:[1,0,1]
	ds_read_b128 v[228:231], v182 offset:21504
	v_pk_fma_f32 v[156:157], v[110:111], v[236:237], v[160:161] op_sel:[0,1,0]
	s_nop 0
	v_pk_fma_f32 v[156:157], v[116:117], v[238:239], v[156:157] op_sel_hi:[1,0,1]
	v_mov_b32_e32 v158, v239
	v_pk_fma_f32 v[160:161], v[120:121], v[158:159], v[156:157] op_sel_hi:[1,0,1]
	s_waitcnt lgkmcnt(2)
	v_pk_fma_f32 v[160:161], v[96:97], v[240:241], v[160:161] op_sel_hi:[1,0,1]
	ds_read_b128 v[232:235], v182 offset:22528
	v_pk_fma_f32 v[156:157], v[98:99], v[240:241], v[160:161] op_sel:[0,1,0]
	s_nop 0
	v_pk_fma_f32 v[156:157], v[102:103], v[242:243], v[156:157] op_sel_hi:[1,0,1]
	v_mov_b32_e32 v158, v243
	v_pk_fma_f32 v[160:161], v[106:107], v[158:159], v[156:157] op_sel_hi:[1,0,1]
	s_waitcnt lgkmcnt(2)
	v_pk_fma_f32 v[160:161], v[92:93], v[224:225], v[160:161] op_sel_hi:[1,0,1]
	ds_read_b128 v[236:239], v182 offset:23552
	v_pk_fma_f32 v[156:157], v[94:95], v[224:225], v[160:161] op_sel:[0,1,0]
	s_nop 0
	v_pk_fma_f32 v[156:157], v[100:101], v[226:227], v[156:157] op_sel_hi:[1,0,1]
	v_mov_b32_e32 v158, v227
	v_pk_fma_f32 v[160:161], v[104:105], v[158:159], v[156:157] op_sel_hi:[1,0,1]
	s_waitcnt lgkmcnt(2)
	v_pk_fma_f32 v[160:161], v[80:81], v[228:229], v[160:161] op_sel_hi:[1,0,1]
	ds_read_b128 v[240:243], v182 offset:24576
	v_pk_fma_f32 v[156:157], v[82:83], v[228:229], v[160:161] op_sel:[0,1,0]
	s_nop 0
	v_pk_fma_f32 v[156:157], v[86:87], v[230:231], v[156:157] op_sel_hi:[1,0,1]
	v_mov_b32_e32 v158, v231
	v_pk_fma_f32 v[160:161], v[90:91], v[158:159], v[156:157] op_sel_hi:[1,0,1]
	s_waitcnt lgkmcnt(2)
	v_pk_fma_f32 v[160:161], v[76:77], v[232:233], v[160:161] op_sel_hi:[1,0,1]
	ds_read_b128 v[224:227], v182 offset:25600
	v_pk_fma_f32 v[156:157], v[78:79], v[232:233], v[160:161] op_sel:[0,1,0]
	s_nop 0
	v_pk_fma_f32 v[156:157], v[84:85], v[234:235], v[156:157] op_sel_hi:[1,0,1]
	v_mov_b32_e32 v158, v235
	v_pk_fma_f32 v[160:161], v[88:89], v[158:159], v[156:157] op_sel_hi:[1,0,1]
	s_waitcnt lgkmcnt(2)
	v_pk_fma_f32 v[160:161], v[68:69], v[236:237], v[160:161] op_sel_hi:[1,0,1]
	ds_read_b128 v[228:231], v182 offset:26624
	v_pk_fma_f32 v[156:157], v[70:71], v[236:237], v[160:161] op_sel:[0,1,0]
	s_nop 0
	v_pk_fma_f32 v[156:157], v[72:73], v[238:239], v[156:157] op_sel_hi:[1,0,1]
	v_mov_b32_e32 v158, v239
	v_pk_fma_f32 v[156:157], v[74:75], v[158:159], v[156:157] op_sel_hi:[1,0,1]
	s_waitcnt lgkmcnt(2)
	v_pk_fma_f32 v[162:163], v[124:125], v[240:241], 0 op_sel_hi:[1,0,0]
	ds_read_b128 v[232:235], v182 offset:27648
	v_pk_fma_f32 v[158:159], v[126:127], v[240:241], v[162:163] op_sel:[0,1,0]
	s_nop 0
	v_pk_fma_f32 v[158:159], v[128:129], v[242:243], v[158:159] op_sel_hi:[1,0,1]
	v_mov_b32_e32 v160, v243
	v_pk_fma_f32 v[162:163], v[130:131], v[160:161], v[158:159] op_sel_hi:[1,0,1]
	s_waitcnt lgkmcnt(2)
	v_pk_fma_f32 v[162:163], v[112:113], v[224:225], v[162:163] op_sel_hi:[1,0,1]
	ds_read_b128 v[236:239], v182 offset:28672
	v_pk_fma_f32 v[158:159], v[114:115], v[224:225], v[162:163] op_sel:[0,1,0]
	s_nop 0
	v_pk_fma_f32 v[158:159], v[118:119], v[226:227], v[158:159] op_sel_hi:[1,0,1]
	v_mov_b32_e32 v160, v227
	v_pk_fma_f32 v[162:163], v[122:123], v[160:161], v[158:159] op_sel_hi:[1,0,1]
	s_waitcnt lgkmcnt(2)
	v_pk_fma_f32 v[162:163], v[108:109], v[228:229], v[162:163] op_sel_hi:[1,0,1]
	ds_read_b128 v[240:243], v182 offset:29696
	v_pk_fma_f32 v[158:159], v[110:111], v[228:229], v[162:163] op_sel:[0,1,0]
	s_nop 0
	v_pk_fma_f32 v[158:159], v[116:117], v[230:231], v[158:159] op_sel_hi:[1,0,1]
	v_mov_b32_e32 v160, v231
	v_pk_fma_f32 v[162:163], v[120:121], v[160:161], v[158:159] op_sel_hi:[1,0,1]
	s_waitcnt lgkmcnt(2)
; #define LAS __attribute__((address_space(3)))
; __device__ __forceinline__ void phase_norm2(const Params& p, const Ctx& F, const int l) {
;     ...
; #pragma unroll
;         for (int e = 0; e < 16; ++e) { f32x2 a = {0.f, 0.f};
; #pragma unroll
;             for (int j = 0; j < 8; ++j) { const f32x4 w = *((const LAS f32x4*)(wr2 + e * DM) + F.lane + 64 * j);
; #pragma unroll
;                 for (int c = 0; c < 4; ++c) a += vv[j][c] * w[c]; }
;             lg[e] = a; }
	v_pk_fma_f32 v[162:163], v[96:97], v[232:233], v[162:163] op_sel_hi:[1,0,1]
	ds_read_b128 v[224:227], v182 offset:30720
	v_pk_fma_f32 v[158:159], v[98:99], v[232:233], v[162:163] op_sel:[0,1,0]
	s_nop 0
	v_pk_fma_f32 v[158:159], v[102:103], v[234:235], v[158:159] op_sel_hi:[1,0,1]
	v_mov_b32_e32 v160, v235
	v_pk_fma_f32 v[162:163], v[106:107], v[160:161], v[158:159] op_sel_hi:[1,0,1]
	s_waitcnt lgkmcnt(2)
	v_pk_fma_f32 v[162:163], v[92:93], v[236:237], v[162:163] op_sel_hi:[1,0,1]
	ds_read_b128 v[228:231], v182 offset:31744
	v_pk_fma_f32 v[158:159], v[94:95], v[236:237], v[162:163] op_sel:[0,1,0]
	s_nop 0
	v_pk_fma_f32 v[158:159], v[100:101], v[238:239], v[158:159] op_sel_hi:[1,0,1]
	v_mov_b32_e32 v160, v239
	v_pk_fma_f32 v[162:163], v[104:105], v[160:161], v[158:159] op_sel_hi:[1,0,1]
	s_waitcnt lgkmcnt(2)
	v_pk_fma_f32 v[162:163], v[80:81], v[240:241], v[162:163] op_sel_hi:[1,0,1]
	ds_read_b128 v[232:235], v182 offset:32768
	v_pk_fma_f32 v[158:159], v[82:83], v[240:241], v[162:163] op_sel:[0,1,0]
	s_nop 0
	v_pk_fma_f32 v[158:159], v[86:87], v[242:243], v[158:159] op_sel_hi:[1,0,1]
	v_mov_b32_e32 v160, v243
	v_pk_fma_f32 v[162:163], v[90:91], v[160:161], v[158:159] op_sel_hi:[1,0,1]
	s_waitcnt lgkmcnt(2)
	v_pk_fma_f32 v[162:163], v[76:77], v[224:225], v[162:163] op_sel_hi:[1,0,1]
	ds_read_b128 v[236:239], v182 offset:33792
	v_pk_fma_f32 v[158:159], v[78:79], v[224:225], v[162:163] op_sel:[0,1,0]
	s_nop 0
	v_pk_fma_f32 v[158:159], v[84:85], v[226:227], v[158:159] op_sel_hi:[1,0,1]
	v_mov_b32_e32 v160, v227
	v_pk_fma_f32 v[162:163], v[88:89], v[160:161], v[158:159] op_sel_hi:[1,0,1]
	s_waitcnt lgkmcnt(2)
	v_pk_fma_f32 v[162:163], v[68:69], v[228:229], v[162:163] op_sel_hi:[1,0,1]
	ds_read_b128 v[240:243], v182 offset:34816
	v_pk_fma_f32 v[158:159], v[70:71], v[228:229], v[162:163] op_sel:[0,1,0]
	s_nop 0
	v_pk_fma_f32 v[158:159], v[72:73], v[230:231], v[158:159] op_sel_hi:[1,0,1]
	v_mov_b32_e32 v160, v231
	v_pk_fma_f32 v[158:159], v[74:75], v[160:161], v[158:159] op_sel_hi:[1,0,1]
	s_waitcnt lgkmcnt(2)
	v_pk_fma_f32 v[164:165], v[124:125], v[232:233], 0 op_sel_hi:[1,0,0]
	ds_read_b128 v[224:227], v182 offset:35840
	v_pk_fma_f32 v[160:161], v[126:127], v[232:233], v[164:165] op_sel:[0,1,0]
	s_nop 0
	v_pk_fma_f32 v[160:161], v[128:129], v[234:235], v[160:161] op_sel_hi:[1,0,1]
	v_mov_b32_e32 v162, v235
	v_pk_fma_f32 v[164:165], v[130:131], v[162:163], v[160:161] op_sel_hi:[1,0,1]
	s_waitcnt lgkmcnt(2)
	v_pk_fma_f32 v[164:165], v[112:113], v[236:237], v[164:165] op_sel_hi:[1,0,1]
	ds_read_b128 v[228:231], v182 offset:36864
	v_pk_fma_f32 v[160:161], v[114:115], v[236:237], v[164:165] op_sel:[0,1,0]
	s_nop 0
	v_pk_fma_f32 v[160:161], v[118:119], v[238:239], v[160:161] op_sel_hi:[1,0,1]
	v_mov_b32_e32 v162, v239
	v_pk_fma_f32 v[164:165], v[122:123], v[162:163], v[160:161] op_sel_hi:[1,0,1]
	s_waitcnt lgkmcnt(2)
	v_pk_fma_f32 v[164:165], v[108:109], v[240:241], v[164:165] op_sel_hi:[1,0,1]
	ds_read_b128 v[232:235], v182 offset:37888
	v_pk_fma_f32 v[160:161], v[110:111], v[240:241], v[164:165] op_sel:[0,1,0]
	s_nop 0
	v_pk_fma_f32 v[160:161], v[116:117], v[242:243], v[160:161] op_sel_hi:[1,0,1]
	v_mov_b32_e32 v162, v243
	v_pk_fma_f32 v[164:165], v[120:121], v[162:163], v[160:161] op_sel_hi:[1,0,1]
	s_waitcnt lgkmcnt(2)
	v_pk_fma_f32 v[164:165], v[96:97], v[224:225], v[164:165] op_sel_hi:[1,0,1]
	ds_read_b128 v[236:239], v182 offset:38912
	v_pk_fma_f32 v[160:161], v[98:99], v[224:225], v[164:165] op_sel:[0,1,0]
	s_nop 0
	v_pk_fma_f32 v[160:161], v[102:103], v[226:227], v[160:161] op_sel_hi:[1,0,1]
	v_mov_b32_e32 v162, v227
	v_pk_fma_f32 v[164:165], v[106:107], v[162:163], v[160:161] op_sel_hi:[1,0,1]
	s_waitcnt lgkmcnt(2)
	v_pk_fma_f32 v[164:165], v[92:93], v[228:229], v[164:165] op_sel_hi:[1,0,1]
	ds_read_b128 v[240:243], v182 offset:39936
	v_pk_fma_f32 v[160:161], v[94:95], v[228:229], v[164:165] op_sel:[0,1,0]
	s_nop 0
	v_pk_fma_f32 v[160:161], v[100:101], v[230:231], v[160:161] op_sel_hi:[1,0,1]
	v_mov_b32_e32 v162, v231
	v_pk_fma_f32 v[164:165], v[104:105], v[162:163], v[160:161] op_sel_hi:[1,0,1]
	s_waitcnt lgkmcnt(2)
	v_pk_fma_f32 v[164:165], v[80:81], v[232:233], v[164:165] op_sel_hi:[1,0,1]
	ds_read_b128 v[224:227], v182 offset:40960
	v_pk_fma_f32 v[160:161], v[82:83], v[232:233], v[164:165] op_sel:[0,1,0]
	s_nop 0
	v_pk_fma_f32 v[160:161], v[86:87], v[234:235], v[160:161] op_sel_hi:[1,0,1]
	v_mov_b32_e32 v162, v235
	v_pk_fma_f32 v[164:165], v[90:91], v[162:163], v[160:161] op_sel_hi:[1,0,1]
	s_waitcnt lgkmcnt(2)
	v_pk_fma_f32 v[164:165], v[76:77], v[236:237], v[164:165] op_sel_hi:[1,0,1]
	ds_read_b128 v[228:231], v182 offset:41984
	v_pk_fma_f32 v[160:161], v[78:79], v[236:237], v[164:165] op_sel:[0,1,0]
	s_nop 0
	v_pk_fma_f32 v[160:161], v[84:85], v[238:239], v[160:161] op_sel_hi:[1,0,1]
	v_mov_b32_e32 v162, v239
	v_pk_fma_f32 v[164:165], v[88:89], v[162:163], v[160:161] op_sel_hi:[1,0,1]
	s_waitcnt lgkmcnt(2)
	v_pk_fma_f32 v[164:165], v[68:69], v[240:241], v[164:165] op_sel_hi:[1,0,1]
	ds_read_b128 v[232:235], v182 offset:43008
	v_pk_fma_f32 v[160:161], v[70:71], v[240:241], v[164:165] op_sel:[0,1,0]
	s_nop 0
	v_pk_fma_f32 v[160:161], v[72:73], v[242:243], v[160:161] op_sel_hi:[1,0,1]
	v_mov_b32_e32 v162, v243
	v_pk_fma_f32 v[160:161], v[74:75], v[162:163], v[160:161] op_sel_hi:[1,0,1]
	s_waitcnt lgkmcnt(2)
	v_pk_fma_f32 v[166:167], v[124:125], v[224:225], 0 op_sel_hi:[1,0,0]
	ds_read_b128 v[236:239], v182 offset:44032
	v_pk_fma_f32 v[162:163], v[126:127], v[224:225], v[166:167] op_sel:[0,1,0]
	s_nop 0
	v_pk_fma_f32 v[162:163], v[128:129], v[226:227], v[162:163] op_sel_hi:[1,0,1]
	v_mov_b32_e32 v164, v227
	v_pk_fma_f32 v[166:167], v[130:131], v[164:165], v[162:163] op_sel_hi:[1,0,1]
	s_waitcnt lgkmcnt(2)
; #define LAS __attribute__((address_space(3)))
; __device__ __forceinline__ void phase_norm2(const Params& p, const Ctx& F, const int l) {
;     ...
;         f32x2 lg[16];
;         unsigned wro = (unsigned)(uintptr_t)wr; asm volatile("" : "+v"(wro));
;         const LAS float* wr2 = (const LAS float*)(uintptr_t)wro;
; #pragma unroll
;         for (int e = 0; e < 16; ++e) { f32x2 a = {0.f, 0.f};
; #pragma unroll
;             for (int j = 0; j < 8; ++j) { const f32x4 w = *((const LAS f32x4*)(wr2 + e * DM) + F.lane + 64 * j);
; #pragma unroll
;                 for (int c = 0; c < 4; ++c) a += vv[j][c] * w[c]; }
;             lg[e] = a; }
	v_pk_fma_f32 v[166:167], v[112:113], v[228:229], v[166:167] op_sel_hi:[1,0,1]
	ds_read_b128 v[240:243], v182 offset:45056
	v_pk_fma_f32 v[162:163], v[114:115], v[228:229], v[166:167] op_sel:[0,1,0]
	s_nop 0
	v_pk_fma_f32 v[162:163], v[118:119], v[230:231], v[162:163] op_sel_hi:[1,0,1]
	v_mov_b32_e32 v164, v231
	v_pk_fma_f32 v[166:167], v[122:123], v[164:165], v[162:163] op_sel_hi:[1,0,1]
	s_waitcnt lgkmcnt(2)
	v_pk_fma_f32 v[166:167], v[108:109], v[232:233], v[166:167] op_sel_hi:[1,0,1]
	ds_read_b128 v[224:227], v182 offset:46080
	v_pk_fma_f32 v[162:163], v[110:111], v[232:233], v[166:167] op_sel:[0,1,0]
	s_nop 0
	v_pk_fma_f32 v[162:163], v[116:117], v[234:235], v[162:163] op_sel_hi:[1,0,1]
	v_mov_b32_e32 v164, v235
	v_pk_fma_f32 v[166:167], v[120:121], v[164:165], v[162:163] op_sel_hi:[1,0,1]
	s_waitcnt lgkmcnt(2)
	v_pk_fma_f32 v[166:167], v[96:97], v[236:237], v[166:167] op_sel_hi:[1,0,1]
	ds_read_b128 v[228:231], v182 offset:47104
	v_pk_fma_f32 v[162:163], v[98:99], v[236:237], v[166:167] op_sel:[0,1,0]
	s_nop 0
	v_pk_fma_f32 v[162:163], v[102:103], v[238:239], v[162:163] op_sel_hi:[1,0,1]
	v_mov_b32_e32 v164, v239
	v_pk_fma_f32 v[166:167], v[106:107], v[164:165], v[162:163] op_sel_hi:[1,0,1]
	s_waitcnt lgkmcnt(2)
	v_pk_fma_f32 v[166:167], v[92:93], v[240:241], v[166:167] op_sel_hi:[1,0,1]
	ds_read_b128 v[232:235], v182 offset:48128
	v_pk_fma_f32 v[162:163], v[94:95], v[240:241], v[166:167] op_sel:[0,1,0]
	s_nop 0
	v_pk_fma_f32 v[162:163], v[100:101], v[242:243], v[162:163] op_sel_hi:[1,0,1]
	v_mov_b32_e32 v164, v243
	v_pk_fma_f32 v[166:167], v[104:105], v[164:165], v[162:163] op_sel_hi:[1,0,1]
	s_waitcnt lgkmcnt(2)
	v_pk_fma_f32 v[166:167], v[80:81], v[224:225], v[166:167] op_sel_hi:[1,0,1]
	ds_read_b128 v[236:239], v182 offset:49152
	v_pk_fma_f32 v[162:163], v[82:83], v[224:225], v[166:167] op_sel:[0,1,0]
	s_nop 0
	v_pk_fma_f32 v[162:163], v[86:87], v[226:227], v[162:163] op_sel_hi:[1,0,1]
	v_mov_b32_e32 v164, v227
	v_pk_fma_f32 v[166:167], v[90:91], v[164:165], v[162:163] op_sel_hi:[1,0,1]
	s_waitcnt lgkmcnt(2)
	v_pk_fma_f32 v[166:167], v[76:77], v[228:229], v[166:167] op_sel_hi:[1,0,1]
	ds_read_b128 v[240:243], v182 offset:50176
	v_pk_fma_f32 v[162:163], v[78:79], v[228:229], v[166:167] op_sel:[0,1,0]
	s_nop 0
	v_pk_fma_f32 v[162:163], v[84:85], v[230:231], v[162:163] op_sel_hi:[1,0,1]
	v_mov_b32_e32 v164, v231
	v_pk_fma_f32 v[166:167], v[88:89], v[164:165], v[162:163] op_sel_hi:[1,0,1]
	s_waitcnt lgkmcnt(2)
	v_pk_fma_f32 v[166:167], v[68:69], v[232:233], v[166:167] op_sel_hi:[1,0,1]
	ds_read_b128 v[224:227], v182 offset:51200
	v_pk_fma_f32 v[162:163], v[70:71], v[232:233], v[166:167] op_sel:[0,1,0]
	s_nop 0
	v_pk_fma_f32 v[162:163], v[72:73], v[234:235], v[162:163] op_sel_hi:[1,0,1]
	v_mov_b32_e32 v164, v235
	v_pk_fma_f32 v[162:163], v[74:75], v[164:165], v[162:163] op_sel_hi:[1,0,1]
	s_waitcnt lgkmcnt(2)
	v_pk_fma_f32 v[168:169], v[124:125], v[236:237], 0 op_sel_hi:[1,0,0]
	ds_read_b128 v[228:231], v182 offset:52224
	v_pk_fma_f32 v[164:165], v[126:127], v[236:237], v[168:169] op_sel:[0,1,0]
	s_nop 0
	v_pk_fma_f32 v[164:165], v[128:129], v[238:239], v[164:165] op_sel_hi:[1,0,1]
	v_mov_b32_e32 v166, v239
	v_pk_fma_f32 v[168:169], v[130:131], v[166:167], v[164:165] op_sel_hi:[1,0,1]
	s_waitcnt lgkmcnt(2)
	v_pk_fma_f32 v[168:169], v[112:113], v[240:241], v[168:169] op_sel_hi:[1,0,1]
	ds_read_b128 v[232:235], v182 offset:53248
	v_pk_fma_f32 v[164:165], v[114:115], v[240:241], v[168:169] op_sel:[0,1,0]
	s_nop 0
	v_pk_fma_f32 v[164:165], v[118:119], v[242:243], v[164:165] op_sel_hi:[1,0,1]
	v_mov_b32_e32 v166, v243
	v_pk_fma_f32 v[168:169], v[122:123], v[166:167], v[164:165] op_sel_hi:[1,0,1]
	s_waitcnt lgkmcnt(2)
	v_pk_fma_f32 v[168:169], v[108:109], v[224:225], v[168:169] op_sel_hi:[1,0,1]
	ds_read_b128 v[236:239], v182 offset:54272
	v_pk_fma_f32 v[164:165], v[110:111], v[224:225], v[168:169] op_sel:[0,1,0]
	s_nop 0
	v_pk_fma_f32 v[164:165], v[116:117], v[226:227], v[164:165] op_sel_hi:[1,0,1]
	v_mov_b32_e32 v166, v227
	v_pk_fma_f32 v[168:169], v[120:121], v[166:167], v[164:165] op_sel_hi:[1,0,1]
	s_waitcnt lgkmcnt(2)
	v_pk_fma_f32 v[168:169], v[96:97], v[228:229], v[168:169] op_sel_hi:[1,0,1]
	ds_read_b128 v[240:243], v182 offset:55296
	v_pk_fma_f32 v[164:165], v[98:99], v[228:229], v[168:169] op_sel:[0,1,0]
	s_nop 0
	v_pk_fma_f32 v[164:165], v[102:103], v[230:231], v[164:165] op_sel_hi:[1,0,1]
	v_mov_b32_e32 v166, v231
	v_pk_fma_f32 v[168:169], v[106:107], v[166:167], v[164:165] op_sel_hi:[1,0,1]
	s_waitcnt lgkmcnt(2)
	v_pk_fma_f32 v[168:169], v[92:93], v[232:233], v[168:169] op_sel_hi:[1,0,1]
	ds_read_b128 v[224:227], v182 offset:56320
	v_pk_fma_f32 v[164:165], v[94:95], v[232:233], v[168:169] op_sel:[0,1,0]
	s_nop 0
	v_pk_fma_f32 v[164:165], v[100:101], v[234:235], v[164:165] op_sel_hi:[1,0,1]
	v_mov_b32_e32 v166, v235
	v_pk_fma_f32 v[168:169], v[104:105], v[166:167], v[164:165] op_sel_hi:[1,0,1]
	s_waitcnt lgkmcnt(2)
	v_pk_fma_f32 v[168:169], v[80:81], v[236:237], v[168:169] op_sel_hi:[1,0,1]
	ds_read_b128 v[228:231], v182 offset:57344
	v_pk_fma_f32 v[164:165], v[82:83], v[236:237], v[168:169] op_sel:[0,1,0]
	s_nop 0
	v_pk_fma_f32 v[164:165], v[86:87], v[238:239], v[164:165] op_sel_hi:[1,0,1]
	v_mov_b32_e32 v166, v239
	v_pk_fma_f32 v[168:169], v[90:91], v[166:167], v[164:165] op_sel_hi:[1,0,1]
	s_waitcnt lgkmcnt(2)
	v_pk_fma_f32 v[168:169], v[76:77], v[240:241], v[168:169] op_sel_hi:[1,0,1]
	ds_read_b128 v[232:235], v182 offset:58368
	v_pk_fma_f32 v[164:165], v[78:79], v[240:241], v[168:169] op_sel:[0,1,0]
	s_nop 0
	v_pk_fma_f32 v[164:165], v[84:85], v[242:243], v[164:165] op_sel_hi:[1,0,1]
	v_mov_b32_e32 v166, v243
	v_pk_fma_f32 v[168:169], v[88:89], v[166:167], v[164:165] op_sel_hi:[1,0,1]
	s_waitcnt lgkmcnt(2)
; #define LAS __attribute__((address_space(3)))
; __device__ __forceinline__ void phase_norm2(const Params& p, const Ctx& F, const int l) {
;     ...
;         f32x2 lg[16];
;         unsigned wro = (unsigned)(uintptr_t)wr; asm volatile("" : "+v"(wro));
;         const LAS float* wr2 = (const LAS float*)(uintptr_t)wro;
; #pragma unroll
;         for (int e = 0; e < 16; ++e) { f32x2 a = {0.f, 0.f};
; #pragma unroll
;             for (int j = 0; j < 8; ++j) { const f32x4 w = *((const LAS f32x4*)(wr2 + e * DM) + F.lane + 64 * j);
; #pragma unroll
;                 for (int c = 0; c < 4; ++c) a += vv[j][c] * w[c]; }
;             lg[e] = a; }
	v_pk_fma_f32 v[168:169], v[68:69], v[224:225], v[168:169] op_sel_hi:[1,0,1]
	ds_read_b128 v[236:239], v182 offset:59392
	v_pk_fma_f32 v[164:165], v[70:71], v[224:225], v[168:169] op_sel:[0,1,0]
	s_nop 0
	v_pk_fma_f32 v[164:165], v[72:73], v[226:227], v[164:165] op_sel_hi:[1,0,1]
	v_mov_b32_e32 v166, v227
	v_pk_fma_f32 v[164:165], v[74:75], v[166:167], v[164:165] op_sel_hi:[1,0,1]
	s_waitcnt lgkmcnt(2)
	v_pk_fma_f32 v[170:171], v[124:125], v[228:229], 0 op_sel_hi:[1,0,0]
	ds_read_b128 v[240:243], v182 offset:60416
	v_pk_fma_f32 v[166:167], v[126:127], v[228:229], v[170:171] op_sel:[0,1,0]
	s_nop 0
	v_pk_fma_f32 v[166:167], v[128:129], v[230:231], v[166:167] op_sel_hi:[1,0,1]
	v_mov_b32_e32 v168, v231
	v_pk_fma_f32 v[170:171], v[130:131], v[168:169], v[166:167] op_sel_hi:[1,0,1]
	s_waitcnt lgkmcnt(2)
	v_pk_fma_f32 v[170:171], v[112:113], v[232:233], v[170:171] op_sel_hi:[1,0,1]
	ds_read_b128 v[224:227], v182 offset:61440
	v_pk_fma_f32 v[166:167], v[114:115], v[232:233], v[170:171] op_sel:[0,1,0]
	s_nop 0
	v_pk_fma_f32 v[166:167], v[118:119], v[234:235], v[166:167] op_sel_hi:[1,0,1]
	v_mov_b32_e32 v168, v235
	v_pk_fma_f32 v[170:171], v[122:123], v[168:169], v[166:167] op_sel_hi:[1,0,1]
	s_waitcnt lgkmcnt(2)
	v_pk_fma_f32 v[170:171], v[108:109], v[236:237], v[170:171] op_sel_hi:[1,0,1]
	ds_read_b128 v[228:231], v182 offset:62464
	v_pk_fma_f32 v[166:167], v[110:111], v[236:237], v[170:171] op_sel:[0,1,0]
	s_nop 0
	v_pk_fma_f32 v[166:167], v[116:117], v[238:239], v[166:167] op_sel_hi:[1,0,1]
	v_mov_b32_e32 v168, v239
	v_pk_fma_f32 v[170:171], v[120:121], v[168:169], v[166:167] op_sel_hi:[1,0,1]
	s_waitcnt lgkmcnt(2)
	v_pk_fma_f32 v[170:171], v[96:97], v[240:241], v[170:171] op_sel_hi:[1,0,1]
	ds_read_b128 v[232:235], v182 offset:63488
	v_pk_fma_f32 v[166:167], v[98:99], v[240:241], v[170:171] op_sel:[0,1,0]
	s_nop 0
	v_pk_fma_f32 v[166:167], v[102:103], v[242:243], v[166:167] op_sel_hi:[1,0,1]
	v_mov_b32_e32 v168, v243
	v_pk_fma_f32 v[170:171], v[106:107], v[168:169], v[166:167] op_sel_hi:[1,0,1]
	s_waitcnt lgkmcnt(2)
	v_pk_fma_f32 v[170:171], v[92:93], v[224:225], v[170:171] op_sel_hi:[1,0,1]
	ds_read_b128 v[236:239], v182 offset:64512
	v_pk_fma_f32 v[166:167], v[94:95], v[224:225], v[170:171] op_sel:[0,1,0]
	s_nop 0
	v_pk_fma_f32 v[166:167], v[100:101], v[226:227], v[166:167] op_sel_hi:[1,0,1]
	v_mov_b32_e32 v168, v227
	v_pk_fma_f32 v[170:171], v[104:105], v[168:169], v[166:167] op_sel_hi:[1,0,1]
	s_waitcnt lgkmcnt(2)
	v_pk_fma_f32 v[170:171], v[80:81], v[228:229], v[170:171] op_sel_hi:[1,0,1]
	ds_read_b128 v[240:243], v244
	v_pk_fma_f32 v[166:167], v[82:83], v[228:229], v[170:171] op_sel:[0,1,0]
	s_nop 0
	v_pk_fma_f32 v[166:167], v[86:87], v[230:231], v[166:167] op_sel_hi:[1,0,1]
	v_mov_b32_e32 v168, v231
	v_pk_fma_f32 v[170:171], v[90:91], v[168:169], v[166:167] op_sel_hi:[1,0,1]
	s_waitcnt lgkmcnt(2)
	v_pk_fma_f32 v[170:171], v[76:77], v[232:233], v[170:171] op_sel_hi:[1,0,1]
	ds_read_b128 v[224:227], v244 offset:1024
	v_pk_fma_f32 v[166:167], v[78:79], v[232:233], v[170:171] op_sel:[0,1,0]
	s_nop 0
	v_pk_fma_f32 v[166:167], v[84:85], v[234:235], v[166:167] op_sel_hi:[1,0,1]
	v_mov_b32_e32 v168, v235
	v_pk_fma_f32 v[170:171], v[88:89], v[168:169], v[166:167] op_sel_hi:[1,0,1]
	s_waitcnt lgkmcnt(2)
	v_pk_fma_f32 v[170:171], v[68:69], v[236:237], v[170:171] op_sel_hi:[1,0,1]
	ds_read_b128 v[228:231], v244 offset:2048
	v_pk_fma_f32 v[166:167], v[70:71], v[236:237], v[170:171] op_sel:[0,1,0]
	s_nop 0
	v_pk_fma_f32 v[166:167], v[72:73], v[238:239], v[166:167] op_sel_hi:[1,0,1]
	v_mov_b32_e32 v168, v239
	v_pk_fma_f32 v[166:167], v[74:75], v[168:169], v[166:167] op_sel_hi:[1,0,1]
	s_waitcnt lgkmcnt(2)
	v_pk_fma_f32 v[172:173], v[124:125], v[240:241], 0 op_sel_hi:[1,0,0]
	ds_read_b128 v[232:235], v244 offset:3072
	v_pk_fma_f32 v[168:169], v[126:127], v[240:241], v[172:173] op_sel:[0,1,0]
	s_nop 0
	v_pk_fma_f32 v[168:169], v[128:129], v[242:243], v[168:169] op_sel_hi:[1,0,1]
	v_mov_b32_e32 v170, v243
	v_pk_fma_f32 v[172:173], v[130:131], v[170:171], v[168:169] op_sel_hi:[1,0,1]
	s_waitcnt lgkmcnt(2)
	v_pk_fma_f32 v[172:173], v[112:113], v[224:225], v[172:173] op_sel_hi:[1,0,1]
	ds_read_b128 v[236:239], v244 offset:4096
	v_pk_fma_f32 v[168:169], v[114:115], v[224:225], v[172:173] op_sel:[0,1,0]
	s_nop 0
	v_pk_fma_f32 v[168:169], v[118:119], v[226:227], v[168:169] op_sel_hi:[1,0,1]
	v_mov_b32_e32 v170, v227
	v_pk_fma_f32 v[172:173], v[122:123], v[170:171], v[168:169] op_sel_hi:[1,0,1]
	s_waitcnt lgkmcnt(2)
	v_pk_fma_f32 v[172:173], v[108:109], v[228:229], v[172:173] op_sel_hi:[1,0,1]
	ds_read_b128 v[240:243], v244 offset:5120
	v_pk_fma_f32 v[168:169], v[110:111], v[228:229], v[172:173] op_sel:[0,1,0]
	s_nop 0
	v_pk_fma_f32 v[168:169], v[116:117], v[230:231], v[168:169] op_sel_hi:[1,0,1]
	v_mov_b32_e32 v170, v231
	v_pk_fma_f32 v[172:173], v[120:121], v[170:171], v[168:169] op_sel_hi:[1,0,1]
	s_waitcnt lgkmcnt(2)
	v_pk_fma_f32 v[172:173], v[96:97], v[232:233], v[172:173] op_sel_hi:[1,0,1]
	ds_read_b128 v[224:227], v244 offset:6144
	v_pk_fma_f32 v[168:169], v[98:99], v[232:233], v[172:173] op_sel:[0,1,0]
	s_nop 0
	v_pk_fma_f32 v[168:169], v[102:103], v[234:235], v[168:169] op_sel_hi:[1,0,1]
	v_mov_b32_e32 v170, v235
	v_pk_fma_f32 v[172:173], v[106:107], v[170:171], v[168:169] op_sel_hi:[1,0,1]
	s_waitcnt lgkmcnt(2)
	v_pk_fma_f32 v[172:173], v[92:93], v[236:237], v[172:173] op_sel_hi:[1,0,1]
	ds_read_b128 v[228:231], v244 offset:7168
	v_pk_fma_f32 v[168:169], v[94:95], v[236:237], v[172:173] op_sel:[0,1,0]
	s_nop 0
	v_pk_fma_f32 v[168:169], v[100:101], v[238:239], v[168:169] op_sel_hi:[1,0,1]
	v_mov_b32_e32 v170, v239
	v_pk_fma_f32 v[172:173], v[104:105], v[170:171], v[168:169] op_sel_hi:[1,0,1]
	s_waitcnt lgkmcnt(2)
; #define LAS __attribute__((address_space(3)))
; __device__ __forceinline__ void phase_norm2(const Params& p, const Ctx& F, const int l) {
;     ...
;         f32x2 lg[16];
;         unsigned wro = (unsigned)(uintptr_t)wr; asm volatile("" : "+v"(wro));
;         const LAS float* wr2 = (const LAS float*)(uintptr_t)wro;
; #pragma unroll
;         for (int e = 0; e < 16; ++e) { f32x2 a = {0.f, 0.f};
; #pragma unroll
;             for (int j = 0; j < 8; ++j) { const f32x4 w = *((const LAS f32x4*)(wr2 + e * DM) + F.lane + 64 * j);
; #pragma unroll
;                 for (int c = 0; c < 4; ++c) a += vv[j][c] * w[c]; }
;             lg[e] = a; }
	v_pk_fma_f32 v[172:173], v[80:81], v[240:241], v[172:173] op_sel_hi:[1,0,1]
	ds_read_b128 v[232:235], v244 offset:8192
	v_pk_fma_f32 v[168:169], v[82:83], v[240:241], v[172:173] op_sel:[0,1,0]
	s_nop 0
	v_pk_fma_f32 v[168:169], v[86:87], v[242:243], v[168:169] op_sel_hi:[1,0,1]
	v_mov_b32_e32 v170, v243
	v_pk_fma_f32 v[172:173], v[90:91], v[170:171], v[168:169] op_sel_hi:[1,0,1]
	s_waitcnt lgkmcnt(2)
	v_pk_fma_f32 v[172:173], v[76:77], v[224:225], v[172:173] op_sel_hi:[1,0,1]
	ds_read_b128 v[236:239], v244 offset:9216
	v_pk_fma_f32 v[168:169], v[78:79], v[224:225], v[172:173] op_sel:[0,1,0]
	s_nop 0
	v_pk_fma_f32 v[168:169], v[84:85], v[226:227], v[168:169] op_sel_hi:[1,0,1]
	v_mov_b32_e32 v170, v227
	v_pk_fma_f32 v[172:173], v[88:89], v[170:171], v[168:169] op_sel_hi:[1,0,1]
	s_waitcnt lgkmcnt(2)
	v_pk_fma_f32 v[172:173], v[68:69], v[228:229], v[172:173] op_sel_hi:[1,0,1]
	ds_read_b128 v[240:243], v244 offset:10240
	v_pk_fma_f32 v[168:169], v[70:71], v[228:229], v[172:173] op_sel:[0,1,0]
	s_nop 0
	v_pk_fma_f32 v[168:169], v[72:73], v[230:231], v[168:169] op_sel_hi:[1,0,1]
	v_mov_b32_e32 v170, v231
	v_pk_fma_f32 v[168:169], v[74:75], v[170:171], v[168:169] op_sel_hi:[1,0,1]
	s_waitcnt lgkmcnt(2)
	v_pk_fma_f32 v[174:175], v[124:125], v[232:233], 0 op_sel_hi:[1,0,0]
	ds_read_b128 v[224:227], v244 offset:11264
	v_pk_fma_f32 v[170:171], v[126:127], v[232:233], v[174:175] op_sel:[0,1,0]
	s_nop 0
	v_pk_fma_f32 v[170:171], v[128:129], v[234:235], v[170:171] op_sel_hi:[1,0,1]
	v_mov_b32_e32 v172, v235
	v_pk_fma_f32 v[174:175], v[130:131], v[172:173], v[170:171] op_sel_hi:[1,0,1]
	s_waitcnt lgkmcnt(2)
	v_pk_fma_f32 v[174:175], v[112:113], v[236:237], v[174:175] op_sel_hi:[1,0,1]
	ds_read_b128 v[228:231], v244 offset:12288
	v_pk_fma_f32 v[170:171], v[114:115], v[236:237], v[174:175] op_sel:[0,1,0]
	s_nop 0
	v_pk_fma_f32 v[170:171], v[118:119], v[238:239], v[170:171] op_sel_hi:[1,0,1]
	v_mov_b32_e32 v172, v239
	v_pk_fma_f32 v[174:175], v[122:123], v[172:173], v[170:171] op_sel_hi:[1,0,1]
	s_waitcnt lgkmcnt(2)
	v_pk_fma_f32 v[174:175], v[108:109], v[240:241], v[174:175] op_sel_hi:[1,0,1]
	ds_read_b128 v[232:235], v244 offset:13312
	v_pk_fma_f32 v[170:171], v[110:111], v[240:241], v[174:175] op_sel:[0,1,0]
	s_nop 0
	v_pk_fma_f32 v[170:171], v[116:117], v[242:243], v[170:171] op_sel_hi:[1,0,1]
	v_mov_b32_e32 v172, v243
	v_pk_fma_f32 v[174:175], v[120:121], v[172:173], v[170:171] op_sel_hi:[1,0,1]
	s_waitcnt lgkmcnt(2)
	v_pk_fma_f32 v[174:175], v[96:97], v[224:225], v[174:175] op_sel_hi:[1,0,1]
	ds_read_b128 v[236:239], v244 offset:14336
	v_pk_fma_f32 v[170:171], v[98:99], v[224:225], v[174:175] op_sel:[0,1,0]
	s_nop 0
	v_pk_fma_f32 v[170:171], v[102:103], v[226:227], v[170:171] op_sel_hi:[1,0,1]
	v_mov_b32_e32 v172, v227
	v_pk_fma_f32 v[174:175], v[106:107], v[172:173], v[170:171] op_sel_hi:[1,0,1]
	s_waitcnt lgkmcnt(2)
	v_pk_fma_f32 v[174:175], v[92:93], v[228:229], v[174:175] op_sel_hi:[1,0,1]
	ds_read_b128 v[240:243], v244 offset:15360
	v_pk_fma_f32 v[170:171], v[94:95], v[228:229], v[174:175] op_sel:[0,1,0]
	s_nop 0
	v_pk_fma_f32 v[170:171], v[100:101], v[230:231], v[170:171] op_sel_hi:[1,0,1]
	v_mov_b32_e32 v172, v231
	v_pk_fma_f32 v[174:175], v[104:105], v[172:173], v[170:171] op_sel_hi:[1,0,1]
	s_waitcnt lgkmcnt(2)
	v_pk_fma_f32 v[174:175], v[80:81], v[232:233], v[174:175] op_sel_hi:[1,0,1]
	ds_read_b128 v[224:227], v244 offset:16384
	v_pk_fma_f32 v[170:171], v[82:83], v[232:233], v[174:175] op_sel:[0,1,0]
	s_nop 0
	v_pk_fma_f32 v[170:171], v[86:87], v[234:235], v[170:171] op_sel_hi:[1,0,1]
	v_mov_b32_e32 v172, v235
	v_pk_fma_f32 v[174:175], v[90:91], v[172:173], v[170:171] op_sel_hi:[1,0,1]
	s_waitcnt lgkmcnt(2)
	v_pk_fma_f32 v[174:175], v[76:77], v[236:237], v[174:175] op_sel_hi:[1,0,1]
	ds_read_b128 v[228:231], v244 offset:17408
	v_pk_fma_f32 v[170:171], v[78:79], v[236:237], v[174:175] op_sel:[0,1,0]
	s_nop 0
	v_pk_fma_f32 v[170:171], v[84:85], v[238:239], v[170:171] op_sel_hi:[1,0,1]
	v_mov_b32_e32 v172, v239
	v_pk_fma_f32 v[174:175], v[88:89], v[172:173], v[170:171] op_sel_hi:[1,0,1]
	s_waitcnt lgkmcnt(2)
	v_pk_fma_f32 v[174:175], v[68:69], v[240:241], v[174:175] op_sel_hi:[1,0,1]
	ds_read_b128 v[232:235], v244 offset:18432
	v_pk_fma_f32 v[170:171], v[70:71], v[240:241], v[174:175] op_sel:[0,1,0]
	s_nop 0
	v_pk_fma_f32 v[170:171], v[72:73], v[242:243], v[170:171] op_sel_hi:[1,0,1]
	v_mov_b32_e32 v172, v243
	v_pk_fma_f32 v[170:171], v[74:75], v[172:173], v[170:171] op_sel_hi:[1,0,1]
	s_waitcnt lgkmcnt(2)
	v_pk_fma_f32 v[176:177], v[124:125], v[224:225], 0 op_sel_hi:[1,0,0]
	ds_read_b128 v[236:239], v244 offset:19456
	v_pk_fma_f32 v[172:173], v[126:127], v[224:225], v[176:177] op_sel:[0,1,0]
	s_nop 0
	v_pk_fma_f32 v[172:173], v[128:129], v[226:227], v[172:173] op_sel_hi:[1,0,1]
	v_mov_b32_e32 v174, v227
	v_pk_fma_f32 v[176:177], v[130:131], v[174:175], v[172:173] op_sel_hi:[1,0,1]
	s_waitcnt lgkmcnt(2)
	v_pk_fma_f32 v[176:177], v[112:113], v[228:229], v[176:177] op_sel_hi:[1,0,1]
	ds_read_b128 v[240:243], v244 offset:20480
	v_pk_fma_f32 v[172:173], v[114:115], v[228:229], v[176:177] op_sel:[0,1,0]
	s_nop 0
	v_pk_fma_f32 v[172:173], v[118:119], v[230:231], v[172:173] op_sel_hi:[1,0,1]
	v_mov_b32_e32 v174, v231
	v_pk_fma_f32 v[176:177], v[122:123], v[174:175], v[172:173] op_sel_hi:[1,0,1]
	s_waitcnt lgkmcnt(2)
	v_pk_fma_f32 v[176:177], v[108:109], v[232:233], v[176:177] op_sel_hi:[1,0,1]
	ds_read_b128 v[224:227], v244 offset:21504
	v_pk_fma_f32 v[172:173], v[110:111], v[232:233], v[176:177] op_sel:[0,1,0]
	s_nop 0
	v_pk_fma_f32 v[172:173], v[116:117], v[234:235], v[172:173] op_sel_hi:[1,0,1]
	v_mov_b32_e32 v174, v235
	v_pk_fma_f32 v[176:177], v[120:121], v[174:175], v[172:173] op_sel_hi:[1,0,1]
	s_waitcnt lgkmcnt(2)
; #define LAS __attribute__((address_space(3)))
; __device__ __forceinline__ void phase_norm2(const Params& p, const Ctx& F, const int l) {
;     ...
;         f32x2 lg[16];
;         unsigned wro = (unsigned)(uintptr_t)wr; asm volatile("" : "+v"(wro));
;         const LAS float* wr2 = (const LAS float*)(uintptr_t)wro;
; #pragma unroll
;         for (int e = 0; e < 16; ++e) { f32x2 a = {0.f, 0.f};
; #pragma unroll
;             for (int j = 0; j < 8; ++j) { const f32x4 w = *((const LAS f32x4*)(wr2 + e * DM) + F.lane + 64 * j);
; #pragma unroll
;                 for (int c = 0; c < 4; ++c) a += vv[j][c] * w[c]; }
;             lg[e] = a; }
	v_pk_fma_f32 v[176:177], v[96:97], v[236:237], v[176:177] op_sel_hi:[1,0,1]
	ds_read_b128 v[228:231], v244 offset:22528
	v_pk_fma_f32 v[172:173], v[98:99], v[236:237], v[176:177] op_sel:[0,1,0]
	s_nop 0
	v_pk_fma_f32 v[172:173], v[102:103], v[238:239], v[172:173] op_sel_hi:[1,0,1]
	v_mov_b32_e32 v174, v239
	v_pk_fma_f32 v[176:177], v[106:107], v[174:175], v[172:173] op_sel_hi:[1,0,1]
	s_waitcnt lgkmcnt(2)
	v_pk_fma_f32 v[176:177], v[92:93], v[240:241], v[176:177] op_sel_hi:[1,0,1]
	ds_read_b128 v[232:235], v244 offset:23552
	v_pk_fma_f32 v[172:173], v[94:95], v[240:241], v[176:177] op_sel:[0,1,0]
	s_nop 0
	v_pk_fma_f32 v[172:173], v[100:101], v[242:243], v[172:173] op_sel_hi:[1,0,1]
	v_mov_b32_e32 v174, v243
	v_pk_fma_f32 v[176:177], v[104:105], v[174:175], v[172:173] op_sel_hi:[1,0,1]
	s_waitcnt lgkmcnt(2)
	v_pk_fma_f32 v[176:177], v[80:81], v[224:225], v[176:177] op_sel_hi:[1,0,1]
	ds_read_b128 v[236:239], v244 offset:24576
	v_pk_fma_f32 v[172:173], v[82:83], v[224:225], v[176:177] op_sel:[0,1,0]
	s_nop 0
	v_pk_fma_f32 v[172:173], v[86:87], v[226:227], v[172:173] op_sel_hi:[1,0,1]
	v_mov_b32_e32 v174, v227
	v_pk_fma_f32 v[176:177], v[90:91], v[174:175], v[172:173] op_sel_hi:[1,0,1]
	s_waitcnt lgkmcnt(2)
	v_pk_fma_f32 v[176:177], v[76:77], v[228:229], v[176:177] op_sel_hi:[1,0,1]
	ds_read_b128 v[240:243], v244 offset:25600
	v_pk_fma_f32 v[172:173], v[78:79], v[228:229], v[176:177] op_sel:[0,1,0]
	s_nop 0
	v_pk_fma_f32 v[172:173], v[84:85], v[230:231], v[172:173] op_sel_hi:[1,0,1]
	v_mov_b32_e32 v174, v231
	v_pk_fma_f32 v[176:177], v[88:89], v[174:175], v[172:173] op_sel_hi:[1,0,1]
	s_waitcnt lgkmcnt(2)
	v_pk_fma_f32 v[176:177], v[68:69], v[232:233], v[176:177] op_sel_hi:[1,0,1]
	ds_read_b128 v[224:227], v244 offset:26624
	v_pk_fma_f32 v[172:173], v[70:71], v[232:233], v[176:177] op_sel:[0,1,0]
	s_nop 0
	v_pk_fma_f32 v[172:173], v[72:73], v[234:235], v[172:173] op_sel_hi:[1,0,1]
	v_mov_b32_e32 v174, v235
	v_pk_fma_f32 v[172:173], v[74:75], v[174:175], v[172:173] op_sel_hi:[1,0,1]
	s_waitcnt lgkmcnt(2)
	v_pk_fma_f32 v[178:179], v[124:125], v[236:237], 0 op_sel_hi:[1,0,0]
	ds_read_b128 v[228:231], v244 offset:27648
	v_pk_fma_f32 v[174:175], v[126:127], v[236:237], v[178:179] op_sel:[0,1,0]
	s_nop 0
	v_pk_fma_f32 v[174:175], v[128:129], v[238:239], v[174:175] op_sel_hi:[1,0,1]
	v_mov_b32_e32 v176, v239
	v_pk_fma_f32 v[178:179], v[130:131], v[176:177], v[174:175] op_sel_hi:[1,0,1]
	s_waitcnt lgkmcnt(2)
	v_pk_fma_f32 v[178:179], v[112:113], v[240:241], v[178:179] op_sel_hi:[1,0,1]
	ds_read_b128 v[232:235], v244 offset:28672
	v_pk_fma_f32 v[174:175], v[114:115], v[240:241], v[178:179] op_sel:[0,1,0]
	s_nop 0
	v_pk_fma_f32 v[174:175], v[118:119], v[242:243], v[174:175] op_sel_hi:[1,0,1]
	v_mov_b32_e32 v176, v243
	v_pk_fma_f32 v[178:179], v[122:123], v[176:177], v[174:175] op_sel_hi:[1,0,1]
	s_waitcnt lgkmcnt(2)
	v_pk_fma_f32 v[178:179], v[108:109], v[224:225], v[178:179] op_sel_hi:[1,0,1]
	ds_read_b128 v[236:239], v244 offset:29696
	v_pk_fma_f32 v[174:175], v[110:111], v[224:225], v[178:179] op_sel:[0,1,0]
	s_nop 0
	v_pk_fma_f32 v[174:175], v[116:117], v[226:227], v[174:175] op_sel_hi:[1,0,1]
	v_mov_b32_e32 v176, v227
	v_pk_fma_f32 v[178:179], v[120:121], v[176:177], v[174:175] op_sel_hi:[1,0,1]
	s_waitcnt lgkmcnt(2)
	v_pk_fma_f32 v[178:179], v[96:97], v[228:229], v[178:179] op_sel_hi:[1,0,1]
	ds_read_b128 v[240:243], v244 offset:30720
	v_pk_fma_f32 v[174:175], v[98:99], v[228:229], v[178:179] op_sel:[0,1,0]
	s_nop 0
	v_pk_fma_f32 v[174:175], v[102:103], v[230:231], v[174:175] op_sel_hi:[1,0,1]
	v_mov_b32_e32 v176, v231
	v_pk_fma_f32 v[178:179], v[106:107], v[176:177], v[174:175] op_sel_hi:[1,0,1]
	s_waitcnt lgkmcnt(2)
	v_pk_fma_f32 v[178:179], v[92:93], v[232:233], v[178:179] op_sel_hi:[1,0,1]
	ds_read_b128 v[224:227], v244 offset:31744
	v_pk_fma_f32 v[174:175], v[94:95], v[232:233], v[178:179] op_sel:[0,1,0]
	s_nop 0
	v_pk_fma_f32 v[174:175], v[100:101], v[234:235], v[174:175] op_sel_hi:[1,0,1]
	v_mov_b32_e32 v176, v235
	v_pk_fma_f32 v[178:179], v[104:105], v[176:177], v[174:175] op_sel_hi:[1,0,1]
	s_waitcnt lgkmcnt(2)
	v_pk_fma_f32 v[178:179], v[80:81], v[236:237], v[178:179] op_sel_hi:[1,0,1]
	ds_read_b128 v[228:231], v244 offset:32768
	v_pk_fma_f32 v[174:175], v[82:83], v[236:237], v[178:179] op_sel:[0,1,0]
	s_nop 0
	v_pk_fma_f32 v[174:175], v[86:87], v[238:239], v[174:175] op_sel_hi:[1,0,1]
	v_mov_b32_e32 v176, v239
	v_pk_fma_f32 v[178:179], v[90:91], v[176:177], v[174:175] op_sel_hi:[1,0,1]
	s_waitcnt lgkmcnt(2)
	v_pk_fma_f32 v[178:179], v[76:77], v[240:241], v[178:179] op_sel_hi:[1,0,1]
	ds_read_b128 v[232:235], v244 offset:33792
	v_pk_fma_f32 v[174:175], v[78:79], v[240:241], v[178:179] op_sel:[0,1,0]
	s_nop 0
	v_pk_fma_f32 v[174:175], v[84:85], v[242:243], v[174:175] op_sel_hi:[1,0,1]
	v_mov_b32_e32 v176, v243
	v_pk_fma_f32 v[178:179], v[88:89], v[176:177], v[174:175] op_sel_hi:[1,0,1]
	s_waitcnt lgkmcnt(2)
	v_pk_fma_f32 v[178:179], v[68:69], v[224:225], v[178:179] op_sel_hi:[1,0,1]
	ds_read_b128 v[236:239], v244 offset:34816
	v_pk_fma_f32 v[174:175], v[70:71], v[224:225], v[178:179] op_sel:[0,1,0]
	s_nop 0
	v_pk_fma_f32 v[174:175], v[72:73], v[226:227], v[174:175] op_sel_hi:[1,0,1]
	v_mov_b32_e32 v176, v227
	v_pk_fma_f32 v[174:175], v[74:75], v[176:177], v[174:175] op_sel_hi:[1,0,1]
	s_waitcnt lgkmcnt(2)
	v_pk_fma_f32 v[180:181], v[124:125], v[228:229], 0 op_sel_hi:[1,0,0]
	ds_read_b128 v[240:243], v244 offset:35840
	v_pk_fma_f32 v[176:177], v[126:127], v[228:229], v[180:181] op_sel:[0,1,0]
	s_nop 0
	v_pk_fma_f32 v[176:177], v[128:129], v[230:231], v[176:177] op_sel_hi:[1,0,1]
	v_mov_b32_e32 v178, v231
	v_pk_fma_f32 v[180:181], v[130:131], v[178:179], v[176:177] op_sel_hi:[1,0,1]
	s_waitcnt lgkmcnt(2)
; #define LAS __attribute__((address_space(3)))
; __device__ __forceinline__ void phase_norm2(const Params& p, const Ctx& F, const int l) {
;     ...
;         f32x2 lg[16];
;         unsigned wro = (unsigned)(uintptr_t)wr; asm volatile("" : "+v"(wro));
;         const LAS float* wr2 = (const LAS float*)(uintptr_t)wro;
; #pragma unroll
;         for (int e = 0; e < 16; ++e) { f32x2 a = {0.f, 0.f};
; #pragma unroll
;             for (int j = 0; j < 8; ++j) { const f32x4 w = *((const LAS f32x4*)(wr2 + e * DM) + F.lane + 64 * j);
; #pragma unroll
;                 for (int c = 0; c < 4; ++c) a += vv[j][c] * w[c]; }
;             lg[e] = a; }
	v_pk_fma_f32 v[180:181], v[112:113], v[232:233], v[180:181] op_sel_hi:[1,0,1]
	ds_read_b128 v[224:227], v244 offset:36864
	v_pk_fma_f32 v[176:177], v[114:115], v[232:233], v[180:181] op_sel:[0,1,0]
	s_nop 0
	v_pk_fma_f32 v[176:177], v[118:119], v[234:235], v[176:177] op_sel_hi:[1,0,1]
	v_mov_b32_e32 v178, v235
	v_pk_fma_f32 v[180:181], v[122:123], v[178:179], v[176:177] op_sel_hi:[1,0,1]
	s_waitcnt lgkmcnt(2)
	v_pk_fma_f32 v[180:181], v[108:109], v[236:237], v[180:181] op_sel_hi:[1,0,1]
	ds_read_b128 v[228:231], v244 offset:37888
	v_pk_fma_f32 v[176:177], v[110:111], v[236:237], v[180:181] op_sel:[0,1,0]
	s_nop 0
	v_pk_fma_f32 v[176:177], v[116:117], v[238:239], v[176:177] op_sel_hi:[1,0,1]
	v_mov_b32_e32 v178, v239
	v_pk_fma_f32 v[180:181], v[120:121], v[178:179], v[176:177] op_sel_hi:[1,0,1]
	s_waitcnt lgkmcnt(2)
	v_pk_fma_f32 v[180:181], v[96:97], v[240:241], v[180:181] op_sel_hi:[1,0,1]
	ds_read_b128 v[232:235], v244 offset:38912
	v_pk_fma_f32 v[176:177], v[98:99], v[240:241], v[180:181] op_sel:[0,1,0]
	s_nop 0
	v_pk_fma_f32 v[176:177], v[102:103], v[242:243], v[176:177] op_sel_hi:[1,0,1]
	v_mov_b32_e32 v178, v243
	v_pk_fma_f32 v[180:181], v[106:107], v[178:179], v[176:177] op_sel_hi:[1,0,1]
	s_waitcnt lgkmcnt(2)
	v_pk_fma_f32 v[180:181], v[92:93], v[224:225], v[180:181] op_sel_hi:[1,0,1]
	ds_read_b128 v[236:239], v244 offset:39936
	v_pk_fma_f32 v[176:177], v[94:95], v[224:225], v[180:181] op_sel:[0,1,0]
	s_nop 0
	v_pk_fma_f32 v[176:177], v[100:101], v[226:227], v[176:177] op_sel_hi:[1,0,1]
	v_mov_b32_e32 v178, v227
	v_pk_fma_f32 v[180:181], v[104:105], v[178:179], v[176:177] op_sel_hi:[1,0,1]
	s_waitcnt lgkmcnt(2)
	v_pk_fma_f32 v[180:181], v[80:81], v[228:229], v[180:181] op_sel_hi:[1,0,1]
	ds_read_b128 v[240:243], v244 offset:40960
	v_pk_fma_f32 v[176:177], v[82:83], v[228:229], v[180:181] op_sel:[0,1,0]
	s_nop 0
	v_pk_fma_f32 v[176:177], v[86:87], v[230:231], v[176:177] op_sel_hi:[1,0,1]
	v_mov_b32_e32 v178, v231
	v_pk_fma_f32 v[180:181], v[90:91], v[178:179], v[176:177] op_sel_hi:[1,0,1]
	s_waitcnt lgkmcnt(2)
	v_pk_fma_f32 v[180:181], v[76:77], v[232:233], v[180:181] op_sel_hi:[1,0,1]
	ds_read_b128 v[224:227], v244 offset:41984
	v_pk_fma_f32 v[176:177], v[78:79], v[232:233], v[180:181] op_sel:[0,1,0]
	s_nop 0
	v_pk_fma_f32 v[176:177], v[84:85], v[234:235], v[176:177] op_sel_hi:[1,0,1]
	v_mov_b32_e32 v178, v235
	v_pk_fma_f32 v[180:181], v[88:89], v[178:179], v[176:177] op_sel_hi:[1,0,1]
	s_waitcnt lgkmcnt(2)
	v_pk_fma_f32 v[180:181], v[68:69], v[236:237], v[180:181] op_sel_hi:[1,0,1]
	ds_read_b128 v[228:231], v244 offset:43008
	v_pk_fma_f32 v[176:177], v[70:71], v[236:237], v[180:181] op_sel:[0,1,0]
	s_nop 0
	v_pk_fma_f32 v[176:177], v[72:73], v[238:239], v[176:177] op_sel_hi:[1,0,1]
	v_mov_b32_e32 v178, v239
	v_pk_fma_f32 v[176:177], v[74:75], v[178:179], v[176:177] op_sel_hi:[1,0,1]
	s_waitcnt lgkmcnt(2)
	v_pk_fma_f32 v[184:185], v[124:125], v[240:241], 0 op_sel_hi:[1,0,0]
	ds_read_b128 v[232:235], v244 offset:44032
	v_pk_fma_f32 v[178:179], v[126:127], v[240:241], v[184:185] op_sel:[0,1,0]
	s_nop 0
	v_pk_fma_f32 v[178:179], v[128:129], v[242:243], v[178:179] op_sel_hi:[1,0,1]
	v_mov_b32_e32 v180, v243
	v_pk_fma_f32 v[184:185], v[130:131], v[180:181], v[178:179] op_sel_hi:[1,0,1]
	s_waitcnt lgkmcnt(2)
	v_pk_fma_f32 v[184:185], v[112:113], v[224:225], v[184:185] op_sel_hi:[1,0,1]
	ds_read_b128 v[236:239], v244 offset:45056
	v_pk_fma_f32 v[178:179], v[114:115], v[224:225], v[184:185] op_sel:[0,1,0]
	s_nop 0
	v_pk_fma_f32 v[178:179], v[118:119], v[226:227], v[178:179] op_sel_hi:[1,0,1]
	v_mov_b32_e32 v180, v227
	v_pk_fma_f32 v[184:185], v[122:123], v[180:181], v[178:179] op_sel_hi:[1,0,1]
	s_waitcnt lgkmcnt(2)
	v_pk_fma_f32 v[184:185], v[108:109], v[228:229], v[184:185] op_sel_hi:[1,0,1]
	ds_read_b128 v[240:243], v244 offset:46080
	v_pk_fma_f32 v[178:179], v[110:111], v[228:229], v[184:185] op_sel:[0,1,0]
	s_nop 0
	v_pk_fma_f32 v[178:179], v[116:117], v[230:231], v[178:179] op_sel_hi:[1,0,1]
	v_mov_b32_e32 v180, v231
	v_pk_fma_f32 v[184:185], v[120:121], v[180:181], v[178:179] op_sel_hi:[1,0,1]
	s_waitcnt lgkmcnt(2)
	v_pk_fma_f32 v[184:185], v[96:97], v[232:233], v[184:185] op_sel_hi:[1,0,1]
	ds_read_b128 v[224:227], v244 offset:47104
	v_pk_fma_f32 v[178:179], v[98:99], v[232:233], v[184:185] op_sel:[0,1,0]
	s_nop 0
	v_pk_fma_f32 v[178:179], v[102:103], v[234:235], v[178:179] op_sel_hi:[1,0,1]
	v_mov_b32_e32 v180, v235
	v_pk_fma_f32 v[184:185], v[106:107], v[180:181], v[178:179] op_sel_hi:[1,0,1]
	s_waitcnt lgkmcnt(2)
	v_pk_fma_f32 v[184:185], v[92:93], v[236:237], v[184:185] op_sel_hi:[1,0,1]
	ds_read_b128 v[228:231], v244 offset:48128
	v_pk_fma_f32 v[178:179], v[94:95], v[236:237], v[184:185] op_sel:[0,1,0]
	s_nop 0
	v_pk_fma_f32 v[178:179], v[100:101], v[238:239], v[178:179] op_sel_hi:[1,0,1]
	v_mov_b32_e32 v180, v239
	v_pk_fma_f32 v[184:185], v[104:105], v[180:181], v[178:179] op_sel_hi:[1,0,1]
	s_waitcnt lgkmcnt(2)
	v_pk_fma_f32 v[184:185], v[80:81], v[240:241], v[184:185] op_sel_hi:[1,0,1]
	ds_read_b128 v[232:235], v244 offset:49152
	v_pk_fma_f32 v[178:179], v[82:83], v[240:241], v[184:185] op_sel:[0,1,0]
	s_nop 0
	v_pk_fma_f32 v[178:179], v[86:87], v[242:243], v[178:179] op_sel_hi:[1,0,1]
	v_mov_b32_e32 v180, v243
	v_pk_fma_f32 v[184:185], v[90:91], v[180:181], v[178:179] op_sel_hi:[1,0,1]
	s_waitcnt lgkmcnt(2)
	v_pk_fma_f32 v[184:185], v[76:77], v[224:225], v[184:185] op_sel_hi:[1,0,1]
	ds_read_b128 v[236:239], v244 offset:50176
	v_pk_fma_f32 v[178:179], v[78:79], v[224:225], v[184:185] op_sel:[0,1,0]
	s_nop 0
	v_pk_fma_f32 v[178:179], v[84:85], v[226:227], v[178:179] op_sel_hi:[1,0,1]
	v_mov_b32_e32 v180, v227
	v_pk_fma_f32 v[184:185], v[88:89], v[180:181], v[178:179] op_sel_hi:[1,0,1]
	s_waitcnt lgkmcnt(2)
; #define LAS __attribute__((address_space(3)))
; __device__ __forceinline__ void phase_norm2(const Params& p, const Ctx& F, const int l) {
;     ...
;         for (int e = 0; e < 16; ++e) { f32x2 a = {0.f, 0.f};
; #pragma unroll
;             for (int j = 0; j < 8; ++j) { const f32x4 w = *((const LAS f32x4*)(wr2 + e * DM) + F.lane + 64 * j);
; #pragma unroll
;                 for (int c = 0; c < 4; ++c) a += vv[j][c] * w[c]; }
;             lg[e] = a; }
;         float lg0[16], lg1[16];
; #pragma unroll
;         for (int e = 0; e < 16; ++e) { lg0[e] = lg[e].x; lg1[e] = lg[e].y; }
	v_pk_fma_f32 v[184:185], v[68:69], v[228:229], v[184:185] op_sel_hi:[1,0,1]
	ds_read_b128 v[240:243], v244 offset:51200
	v_pk_fma_f32 v[178:179], v[70:71], v[228:229], v[184:185] op_sel:[0,1,0]
	v_pk_fma_f32 v[178:179], v[72:73], v[230:231], v[178:179] op_sel_hi:[1,0,1]
	v_mov_b32_e32 v180, v231
	v_pk_fma_f32 v[178:179], v[74:75], v[180:181], v[178:179] op_sel_hi:[1,0,1]
	s_waitcnt lgkmcnt(2)
	v_pk_fma_f32 v[180:181], v[124:125], v[232:233], 0 op_sel_hi:[1,0,0]
	ds_read_b128 v[224:227], v244 offset:52224
	v_pk_fma_f32 v[180:181], v[126:127], v[232:233], v[180:181] op_sel:[0,1,0]
	v_mov_b32_e32 v184, v235
	v_pk_fma_f32 v[180:181], v[128:129], v[234:235], v[180:181] op_sel_hi:[1,0,1]
	s_nop 0
	v_pk_fma_f32 v[180:181], v[130:131], v[184:185], v[180:181] op_sel_hi:[1,0,1]
	s_waitcnt lgkmcnt(2)
	v_pk_fma_f32 v[180:181], v[112:113], v[236:237], v[180:181] op_sel_hi:[1,0,1]
	ds_read_b128 v[228:231], v244 offset:53248
	v_pk_fma_f32 v[180:181], v[114:115], v[236:237], v[180:181] op_sel:[0,1,0]
	v_mov_b32_e32 v184, v239
	v_pk_fma_f32 v[180:181], v[118:119], v[238:239], v[180:181] op_sel_hi:[1,0,1]
	s_nop 0
	v_pk_fma_f32 v[180:181], v[122:123], v[184:185], v[180:181] op_sel_hi:[1,0,1]
	s_waitcnt lgkmcnt(2)
	v_pk_fma_f32 v[180:181], v[108:109], v[240:241], v[180:181] op_sel_hi:[1,0,1]
	ds_read_b128 v[232:235], v244 offset:54272
	v_pk_fma_f32 v[180:181], v[110:111], v[240:241], v[180:181] op_sel:[0,1,0]
	v_mov_b32_e32 v184, v243
	v_pk_fma_f32 v[180:181], v[116:117], v[242:243], v[180:181] op_sel_hi:[1,0,1]
	s_nop 0
	v_pk_fma_f32 v[180:181], v[120:121], v[184:185], v[180:181] op_sel_hi:[1,0,1]
	s_waitcnt lgkmcnt(2)
	v_pk_fma_f32 v[180:181], v[96:97], v[224:225], v[180:181] op_sel_hi:[1,0,1]
	ds_read_b128 v[236:239], v244 offset:55296
	v_pk_fma_f32 v[180:181], v[98:99], v[224:225], v[180:181] op_sel:[0,1,0]
	v_mov_b32_e32 v184, v227
	v_pk_fma_f32 v[180:181], v[102:103], v[226:227], v[180:181] op_sel_hi:[1,0,1]
	s_nop 0
	v_pk_fma_f32 v[180:181], v[106:107], v[184:185], v[180:181] op_sel_hi:[1,0,1]
	s_waitcnt lgkmcnt(2)
	v_pk_fma_f32 v[180:181], v[92:93], v[228:229], v[180:181] op_sel_hi:[1,0,1]
	ds_read_b128 v[240:243], v244 offset:56320
	v_pk_fma_f32 v[180:181], v[94:95], v[228:229], v[180:181] op_sel:[0,1,0]
	v_mov_b32_e32 v184, v231
	v_pk_fma_f32 v[180:181], v[100:101], v[230:231], v[180:181] op_sel_hi:[1,0,1]
	s_nop 0
	v_pk_fma_f32 v[180:181], v[104:105], v[184:185], v[180:181] op_sel_hi:[1,0,1]
	s_waitcnt lgkmcnt(2)
	v_pk_fma_f32 v[180:181], v[80:81], v[232:233], v[180:181] op_sel_hi:[1,0,1]
	ds_read_b128 v[224:227], v244 offset:57344
	v_pk_fma_f32 v[180:181], v[82:83], v[232:233], v[180:181] op_sel:[0,1,0]
	v_mov_b32_e32 v184, v235
	v_pk_fma_f32 v[180:181], v[86:87], v[234:235], v[180:181] op_sel_hi:[1,0,1]
	s_nop 0
	v_pk_fma_f32 v[180:181], v[90:91], v[184:185], v[180:181] op_sel_hi:[1,0,1]
	s_waitcnt lgkmcnt(2)
	v_pk_fma_f32 v[180:181], v[76:77], v[236:237], v[180:181] op_sel_hi:[1,0,1]
	ds_read_b128 v[228:231], v244 offset:58368
	v_pk_fma_f32 v[180:181], v[78:79], v[236:237], v[180:181] op_sel:[0,1,0]
	v_mov_b32_e32 v184, v239
	v_pk_fma_f32 v[180:181], v[84:85], v[238:239], v[180:181] op_sel_hi:[1,0,1]
	s_nop 0
	v_pk_fma_f32 v[180:181], v[88:89], v[184:185], v[180:181] op_sel_hi:[1,0,1]
	s_waitcnt lgkmcnt(2)
	v_pk_fma_f32 v[180:181], v[68:69], v[240:241], v[180:181] op_sel_hi:[1,0,1]
	ds_read_b128 v[232:235], v244 offset:59392
	v_pk_fma_f32 v[180:181], v[70:71], v[240:241], v[180:181] op_sel:[0,1,0]
	v_mov_b32_e32 v184, v243
	v_pk_fma_f32 v[180:181], v[72:73], v[242:243], v[180:181] op_sel_hi:[1,0,1]
	s_nop 0
	v_pk_fma_f32 v[180:181], v[74:75], v[184:185], v[180:181] op_sel_hi:[1,0,1]
	s_waitcnt lgkmcnt(2)
	v_pk_fma_f32 v[124:125], v[124:125], v[224:225], 0 op_sel_hi:[1,0,0]
	ds_read_b128 v[236:239], v244 offset:60416
	v_pk_fma_f32 v[124:125], v[126:127], v[224:225], v[124:125] op_sel:[0,1,0]
	v_mov_b32_e32 v126, v227
	v_pk_fma_f32 v[124:125], v[128:129], v[226:227], v[124:125] op_sel_hi:[1,0,1]
	s_nop 0
	v_pk_fma_f32 v[128:129], v[130:131], v[126:127], v[124:125] op_sel_hi:[1,0,1]
	s_waitcnt lgkmcnt(2)
	v_pk_fma_f32 v[112:113], v[112:113], v[228:229], v[128:129] op_sel_hi:[1,0,1]
	ds_read_b128 v[240:243], v244 offset:61440
	v_pk_fma_f32 v[112:113], v[114:115], v[228:229], v[112:113] op_sel:[0,1,0]
	v_mov_b32_e32 v114, v231
	v_pk_fma_f32 v[112:113], v[118:119], v[230:231], v[112:113] op_sel_hi:[1,0,1]
	s_nop 0
	v_pk_fma_f32 v[118:119], v[122:123], v[114:115], v[112:113] op_sel_hi:[1,0,1]
	s_waitcnt lgkmcnt(2)
	v_pk_fma_f32 v[108:109], v[108:109], v[232:233], v[118:119] op_sel_hi:[1,0,1]
	ds_read_b128 v[224:227], v244 offset:62464
	v_pk_fma_f32 v[108:109], v[110:111], v[232:233], v[108:109] op_sel:[0,1,0]
	v_mov_b32_e32 v110, v235
	v_pk_fma_f32 v[108:109], v[116:117], v[234:235], v[108:109] op_sel_hi:[1,0,1]
	s_nop 0
	v_pk_fma_f32 v[112:113], v[120:121], v[110:111], v[108:109] op_sel_hi:[1,0,1]
	s_waitcnt lgkmcnt(2)
	v_pk_fma_f32 v[96:97], v[96:97], v[236:237], v[112:113] op_sel_hi:[1,0,1]
	ds_read_b128 v[228:231], v244 offset:63488
	v_pk_fma_f32 v[96:97], v[98:99], v[236:237], v[96:97] op_sel:[0,1,0]
	v_mov_b32_e32 v98, v239
	v_pk_fma_f32 v[96:97], v[102:103], v[238:239], v[96:97] op_sel_hi:[1,0,1]
	s_nop 0
	v_pk_fma_f32 v[102:103], v[106:107], v[98:99], v[96:97] op_sel_hi:[1,0,1]
	s_waitcnt lgkmcnt(2)
; #define LAS __attribute__((address_space(3)))
; __device__ __forceinline__ void router_tail(const Ctx& F, const float (&lg)[16], const int b, const int t, const bool valid) {
;     const bool b5 = (F.lane & 32) != 0, b4 = (F.lane & 16) != 0, b3 = (F.lane & 8) != 0, b2 = (F.lane & 4) != 0;
;     float r8[8], r4[4], r2[2];
; #pragma unroll
;     for (int e = 0; e < 8; ++e) { const float keep = b5 ? lg[e + 8] : lg[e], send = b5 ? lg[e] : lg[e + 8]; r8[e] = keep + __shfl_xor(send, 32); }
; #pragma unroll
;     for (int e = 0; e < 4; ++e) { const float keep = b4 ? r8[e + 4] : r8[e], send = b4 ? r8[e] : r8[e + 4]; r4[e] = keep + __shfl_xor(send, 16); }
; #pragma unroll
;     for (int e = 0; e < 2; ++e) { const float keep = b3 ? r4[e + 2] : r4[e], send = b3 ? r4[e] : r4[e + 2]; r2[e] = keep + __shfl_xor(send, 8); }
;     float lgt; { const float keep = b2 ? r2[1] : r2[0], send = b2 ? r2[0] : r2[1]; lgt = keep + __shfl_xor(send, 4); }
;     lgt += __shfl_xor(lgt, 2); lgt += __shfl_xor(lgt, 1);
;     float mx = lgt;
;     mx = fmaxf(mx, __shfl_xor(mx, 4)); mx = fmaxf(mx, __shfl_xor(mx, 8)); mx = fmaxf(mx, __shfl_xor(mx, 16)); mx = fmaxf(mx, __shfl_xor(mx, 32));
;     const float ex = expf(lgt - mx); float sum = ex;
;     sum += __shfl_xor(sum, 4); sum += __shfl_xor(sum, 8); sum += __shfl_xor(sum, 16); sum += __shfl_xor(sum, 32);
;     if (valid && (F.lane & 3) == 0) { const float af = ex / sum; const int e = F.lane >> 2;
;         if (t < CTXL) F.affc[((size_t)(b * 16 + e)) * CTXL + t] = af; else F.affl[((size_t)(b * 16 + e)) * SEQ + (t - CTXL)] = af; }
; __device__ __forceinline__ void phase_norm2(const Params& p, const Ctx& F, const int l) {
;     ...
;         for (int e = 0; e < 16; ++e) { f32x2 a = {0.f, 0.f};
; #pragma unroll
;             for (int j = 0; j < 8; ++j) { const f32x4 w = *((const LAS f32x4*)(wr2 + e * DM) + F.lane + 64 * j);
; #pragma unroll
;                 for (int c = 0; c < 4; ++c) a += vv[j][c] * w[c]; }
;             lg[e] = a; }
;         float lg0[16], lg1[16];
; #pragma unroll
;         for (int e = 0; e < 16; ++e) { lg0[e] = lg[e].x; lg1[e] = lg[e].y; }
	v_pk_fma_f32 v[92:93], v[92:93], v[240:241], v[102:103] op_sel_hi:[1,0,1]
	ds_read_b128 v[232:235], v244 offset:64512
	v_pk_fma_f32 v[92:93], v[94:95], v[240:241], v[92:93] op_sel:[0,1,0]
	v_mov_b32_e32 v94, v243
	v_pk_fma_f32 v[92:93], v[100:101], v[242:243], v[92:93] op_sel_hi:[1,0,1]
	s_nop 0
	v_pk_fma_f32 v[96:97], v[104:105], v[94:95], v[92:93] op_sel_hi:[1,0,1]
	s_waitcnt lgkmcnt(2)
	v_pk_fma_f32 v[80:81], v[80:81], v[224:225], v[96:97] op_sel_hi:[1,0,1]
	s_nop 0
	v_pk_fma_f32 v[80:81], v[82:83], v[224:225], v[80:81] op_sel:[0,1,0]
	v_mov_b32_e32 v82, v227
	v_pk_fma_f32 v[80:81], v[86:87], v[226:227], v[80:81] op_sel_hi:[1,0,1]
	s_nop 0
	v_pk_fma_f32 v[86:87], v[90:91], v[82:83], v[80:81] op_sel_hi:[1,0,1]
	s_waitcnt lgkmcnt(1)
	v_pk_fma_f32 v[76:77], v[76:77], v[228:229], v[86:87] op_sel_hi:[1,0,1]
	s_nop 0
	v_pk_fma_f32 v[76:77], v[78:79], v[228:229], v[76:77] op_sel:[0,1,0]
	v_mov_b32_e32 v78, v231
	v_pk_fma_f32 v[76:77], v[84:85], v[230:231], v[76:77] op_sel_hi:[1,0,1]
	s_nop 0
	v_pk_fma_f32 v[80:81], v[88:89], v[78:79], v[76:77] op_sel_hi:[1,0,1]
	v_cndmask_b32_e64 v1, v168, v152, s[38:39]
	s_waitcnt lgkmcnt(0)
	v_pk_fma_f32 v[68:69], v[68:69], v[232:233], v[80:81] op_sel_hi:[1,0,1]
	s_nop 0
	v_pk_fma_f32 v[68:69], v[70:71], v[232:233], v[68:69] op_sel:[0,1,0]
	v_mov_b32_e32 v70, v235
	v_pk_fma_f32 v[68:69], v[72:73], v[234:235], v[68:69] op_sel_hi:[1,0,1]
	v_cndmask_b32_e64 v72, v156, v172, s[38:39]
	v_pk_fma_f32 v[68:69], v[74:75], v[70:71], v[68:69] op_sel_hi:[1,0,1]
	s_nop 1
	v_permlane32_swap_b32_e32 v152, v168
	v_permlane32_swap_b32_e32 v154, v170
	v_permlane32_swap_b32_e32 v156, v172
	v_permlane32_swap_b32_e32 v158, v174
	v_permlane32_swap_b32_e32 v160, v176
	v_permlane32_swap_b32_e32 v162, v178
	v_permlane32_swap_b32_e32 v164, v180
	v_permlane32_swap_b32_e32 v166, v68
	v_add_f32_e32 v1, v152, v168
	v_add_f32_e32 v70, v154, v170
	v_add_f32_e32 v71, v156, v172
	v_add_f32_e32 v72, v158, v174
	v_add_f32_e32 v73, v160, v176
	v_add_f32_e32 v74, v162, v178
	v_add_f32_e32 v75, v164, v180
	v_add_f32_e32 v68, v166, v68
	s_waitcnt lgkmcnt(0)
	v_cndmask_b32_e64 v76, v73, v1, s[40:41]
	v_cndmask_b32_e64 v1, v1, v73, s[40:41]
	v_cndmask_b32_e64 v73, v74, v70, s[40:41]
	v_cndmask_b32_e64 v70, v70, v74, s[40:41]
	ds_bpermute_b32 v70, v193, v70
	ds_bpermute_b32 v1, v193, v1
	s_waitcnt lgkmcnt(1)
	v_add_f32_e32 v70, v73, v70
	v_cndmask_b32_e64 v73, v75, v71, s[40:41]
	v_cndmask_b32_e64 v71, v71, v75, s[40:41]
	ds_bpermute_b32 v71, v193, v71
	s_waitcnt lgkmcnt(1)
	v_add_f32_e32 v1, v76, v1
	s_waitcnt lgkmcnt(0)
	v_add_f32_e32 v71, v73, v71
	v_cndmask_b32_e64 v73, v68, v72, s[40:41]
	v_cndmask_b32_e64 v68, v72, v68, s[40:41]
	ds_bpermute_b32 v68, v193, v68
	v_cndmask_b32_e64 v72, v71, v1, s[42:43]
	v_cndmask_b32_e64 v1, v1, v71, s[42:43]
	ds_bpermute_b32 v1, v192, v1
	s_waitcnt lgkmcnt(1)
	v_add_f32_e32 v68, v73, v68
	v_cndmask_b32_e64 v71, v68, v70, s[42:43]
	v_cndmask_b32_e64 v68, v70, v68, s[42:43]
	ds_bpermute_b32 v68, v192, v68
	s_waitcnt lgkmcnt(1)
	v_add_f32_e32 v1, v72, v1
	s_waitcnt lgkmcnt(0)
	v_add_f32_e32 v68, v71, v68
	v_cndmask_b32_e64 v70, v68, v1, s[4:5]
	v_cndmask_b32_e64 v1, v1, v68, s[4:5]
	ds_bpermute_b32 v1, v191, v1
	s_waitcnt lgkmcnt(0)
	v_add_f32_e32 v1, v70, v1
	s_nop 1
	v_add_f32_dpp v1, v1, v1 quad_perm:[2,3,0,1] row_mask:0xf bank_mask:0xf
	s_nop 1
	v_add_f32_dpp v1, v1, v1 quad_perm:[1,0,3,2] row_mask:0xf bank_mask:0xf
	s_nop 1
	v_max_f32_dpp v68, v1, v1 row_half_mirror row_mask:0xf bank_mask:0xf
	s_nop 1
	v_max_f32_dpp v68, v68, v68 row_mirror row_mask:0xf bank_mask:0xf
	v_mov_b32_e32 v70, v68
	s_nop 1
	v_permlane16_swap_b32_e32 v68, v70
	v_max_f32_e32 v68, v68, v70
	v_mov_b32_e32 v70, v68
	s_nop 1
	v_permlane32_swap_b32_e32 v68, v70
	v_max_f32_e32 v68, v68, v70
	v_sub_f32_e32 v1, v1, v68
	v_mul_f32_e32 v68, 0x3fb8aa3b, v1
	v_fma_f32 v70, v1, s55, -v68
	v_rndne_f32_e32 v71, v68
	v_fmac_f32_e32 v70, 0x32a5705f, v1
	v_sub_f32_e32 v68, v68, v71
	v_add_f32_e32 v68, v68, v70
	v_exp_f32_e32 v68, v68
	v_cvt_i32_f32_e32 v70, v71
	v_cmp_ngt_f32_e32 vcc, s56, v1
	v_ldexp_f32 v68, v68, v70
	s_nop 0
	v_cndmask_b32_e32 v68, 0, v68, vcc
	v_cmp_nlt_f32_e32 vcc, s57, v1
	s_nop 1
	v_cndmask_b32_e32 v68, v222, v68, vcc
	s_nop 1
	v_add_f32_dpp v1, v68, v68 row_half_mirror row_mask:0xf bank_mask:0xf
	s_nop 1
	v_add_f32_dpp v1, v1, v1 row_mirror row_mask:0xf bank_mask:0xf
	v_mov_b32_e32 v70, v1
	s_nop 1
	v_permlane16_swap_b32_e32 v1, v70
	v_add_f32_e32 v70, v1, v70
	ds_bpermute_b32 v71, v194, v70
	s_and_saveexec_b64 s[0:1], s[6:7]
	s_cbranch_execz .LBB0_942
	s_waitcnt lgkmcnt(0)
	v_add_f32_e32 v1, v70, v71
	v_div_scale_f32 v70, s[12:13], v1, v1, v68
	v_rcp_f32_e32 v71, v70
	v_div_scale_f32 v72, vcc, v68, v1, v68
	s_cmpk_gt_i32 s60, 0xff
	v_fma_f32 v73, -v70, v71, 1.0
	v_fmac_f32_e32 v71, v73, v71
	v_mul_f32_e32 v73, v72, v71
	v_fma_f32 v74, -v70, v73, v72
	v_fmac_f32_e32 v73, v74, v71
	v_fma_f32 v70, -v70, v73, v72
	v_div_fmas_f32 v70, v70, v71, v73
	v_div_fixup_f32 v68, v70, v1, v68
	s_mov_b64 s[12:13], -1
	s_cbranch_scc0 .LBB0_940
	v_lshl_add_u64 v[70:71], s[60:61], 2, v[148:149]
	global_store_dword v[70:71], v68, off offset:-1024
	s_mov_b64 s[12:13], 0
